# speedup vs baseline: 1.0847x; 1.0103x over previous
_Z6k_prepPKiPKfPiS3_P15HIP_vector_typeIjLj4EEPh:
	s_mov_b64 s[4:5], -1
	s_cmpk_lt_i32 s2, 10
	v_lshl_or_b32 v2, s2, 9, v0
	s_cbranch_scc0 .LBB0_20
	v_mov_b32_e32 v3, v2
	s_movk_i32 s3, 0x1300
	v_cmp_gt_i32_e32 vcc, s3, v3
	s_and_saveexec_b64 s[4:5], vcc
	s_cbranch_execz .LBB0_19
	s_load_dwordx2 s[6:7], s[0:1], 0x8
	s_load_dwordx2 s[8:9], s[0:1], 0x20
	v_bfe_u32 v1, v0, 6, 2
	v_and_b32_e32 v4, 15, v0
	v_lshl_or_b32 v4, v1, 4, v4
	v_lshrrev_b32_e32 v5, 1, v0
	v_lshrrev_b32_e32 v3, 8, v3
	v_and_b32_e32 v5, 24, v5
	v_mul_u32_u24_e32 v4, 0x4b0, v4
	v_lshl_or_b32 v8, v3, 5, v5
	v_lshlrev_b32_e32 v4, 2, v4
	v_mov_b32_e32 v5, 0
	s_movk_i32 s3, 0x258
	v_mov_b32_e32 v9, 0
	v_mov_b32_e32 v12, 0
	v_mov_b32_e32 v13, 0
	v_mov_b32_e32 v14, 0
	v_mov_b32_e32 v15, 0
	v_mov_b32_e32 v16, 0
	v_mov_b32_e32 v17, 0
	v_mov_b32_e32 v18, 0
	v_mov_b32_e32 v19, 0
	v_mov_b32_e32 v20, 0
	v_mov_b32_e32 v21, 0
	v_mov_b32_e32 v22, 0
	v_mov_b32_e32 v23, 0
	v_mov_b32_e32 v24, 0
	v_mov_b32_e32 v25, 0
	v_mov_b32_e32 v26, 0
	v_mov_b32_e32 v27, 0
	s_waitcnt lgkmcnt(0)
	v_lshl_add_u64 v[6:7], s[6:7], 0, v[4:5]
	v_cmp_gt_u32_e32 vcc, s3, v8
	v_lshlrev_b32_e32 v8, 3, v8
	v_lshl_add_u64 v[10:11], v[6:7], 0, v[8:9]
	s_and_saveexec_b64 s[6:7], vcc
	global_load_dwordx4 v[12:15], v[10:11], off
	global_load_dwordx4 v[16:19], v[10:11], off offset:16
	global_load_dwordx4 v[20:23], v[10:11], off offset:32
	global_load_dwordx4 v[24:27], v[10:11], off offset:48
	s_or_b64 exec, exec, s[6:7]
	v_and_b32_e32 v4, 63, v0
	v_lshlrev_b32_e32 v3, 9, v3
	v_lshlrev_b32_e32 v1, 6, v1
	v_or3_b32 v4, v3, v1, v4
	v_mov_b32_e32 v5, 0
	v_lshl_add_u64 v[10:11], v[4:5], 4, s[8:9]
	v_add_u32_e32 v4, 0x100, v4
	v_lshl_add_u64 v[4:5], v[4:5], 4, s[8:9]
	s_waitcnt vmcnt(0)
	v_cvt_pk_f16_f32 v28, v12, v14
	v_cvt_pk_f16_f32 v29, v16, v18
	v_cvt_pk_f16_f32 v30, v20, v22
	v_cvt_pk_f16_f32 v31, v24, v26
	v_cvt_pk_f16_f32 v32, v13, v15
	v_cvt_pk_f16_f32 v33, v17, v19
	v_cvt_pk_f16_f32 v34, v21, v23
	v_cvt_pk_f16_f32 v35, v25, v27
	global_store_dwordx4 v[10:11], v[28:31], off
	global_store_dwordx4 v[4:5], v[32:35], off

.LBB0_20:
	s_andn2_b64 vcc, exec, s[4:5]
	s_cbranch_vccnz .LBB0_27
	s_load_dwordx2 s[4:5], s[0:1], 0x0
	s_load_dwordx2 s[6:7], s[0:1], 0x18
	s_sub_u32 s2, s2, 10
	v_lshl_or_b32 v2, s2, 9, v0
	v_lshl_add_u32 v4, v0, 8, s2
	v_ashrrev_i32_e32 v5, 31, v4
	v_ashrrev_i32_e32 v3, 31, v2
	s_waitcnt lgkmcnt(0)
	v_lshl_add_u64 v[4:5], v[4:5], 2, s[4:5]
	global_load_dword v4, v[4:5], off
	v_and_b32_e32 v1, 63, v0
	v_lshl_add_u64 v[2:3], v[2:3], 2, s[6:7]
	v_cmp_eq_u32_e64 s[4:5], 0, v1
	s_waitcnt vmcnt(0)
	v_cmp_ne_u32_e32 vcc, 1, v4
	global_store_dword v[2:3], v4, off
	s_and_saveexec_b64 s[6:7], s[4:5]
	s_bcnt1_i32_b64 s3, vcc
	v_lshrrev_b32_e32 v1, 4, v0
	v_mov_b32_e32 v2, s3
	ds_write_b32 v1, v2
	s_or_b64 exec, exec, s[6:7]
	v_mov_b32_e32 v1, 0
	s_waitcnt lgkmcnt(0)
	s_barrier
	ds_read_b128 v[6:9], v1
	ds_read_b128 v[10:13], v1 offset:16
	v_cmp_eq_u32_e32 vcc, 0, v0
	s_waitcnt lgkmcnt(1)
	v_add_u32_e32 v2, v7, v6
	v_add_u32_e32 v2, v8, v2
	v_add_u32_e32 v2, v9, v2
	s_waitcnt lgkmcnt(0)
	v_add_u32_e32 v2, v10, v2
	v_add_u32_e32 v2, v11, v2
	v_add_u32_e32 v2, v12, v2
	v_add_u32_e32 v2, v13, v2
	s_and_saveexec_b64 s[4:5], vcc
	s_cbranch_execz .LBB0_25
	s_load_dwordx2 s[6:7], s[0:1], 0x10
	s_ashr_i32 s3, s2, 31
	s_lshl_b64 s[2:3], s[2:3], 2
	s_waitcnt lgkmcnt(0)
	s_add_u32 s2, s6, s2
	s_addc_u32 s3, s7, s3
	global_store_dword v1, v2, s[2:3]
